# speedup vs baseline: 1.0421x; 1.0421x over previous
.LBB0_7:
	s_add_i32 s12, s10, s6
	s_cmp_gt_i32 s6, 0
	s_load_dwordx2 s[8:9], s[0:1], 0x18
	s_cselect_b64 s[6:7], -1, 0
	v_bfe_u32 v1, v0, 3, 4
	s_lshl_b32 s10, s10, 4
	v_or_b32_e32 v2, s10, v1
	v_lshlrev_b32_e32 v34, 8, v2
	s_lshl_b32 s12, s12, 4
	v_lshlrev_b32_e32 v2, 1, v0
	s_lshl_b32 s14, s2, 22
	v_mov_b32_e32 v35, 0
	v_and_b32_e32 v36, 14, v2
	v_or_b32_e32 v2, s12, v1
	v_lshrrev_b32_e32 v37, 7, v0
	s_and_b32 s14, s14, 0x1c00000
	v_lshlrev_b32_e32 v2, 8, v2
	v_lshl_or_b32 v4, v37, 19, s14
	v_mov_b32_e32 v5, v35
	s_ashr_i32 s13, s12, 31
	v_ashrrev_i32_e32 v3, 31, v2
	s_waitcnt lgkmcnt(0)
	v_lshl_add_u64 v[4:5], s[8:9], 0, v[4:5]
	v_lshlrev_b64 v[26:27], 3, v[34:35]
	s_mov_b32 s11, 0
	v_lshl_add_u64 v[6:7], v[4:5], 0, v[26:27]
	s_lshl_b64 s[12:13], s[12:13], 3
	v_lshlrev_b64 v[28:29], 3, v[2:3]
	v_lshl_add_u64 v[6:7], v[6:7], 0, s[12:13]
	v_lshlrev_b32_e32 v34, 3, v36
	v_lshl_add_u64 v[2:3], v[4:5], 0, v[28:29]
	s_lshl_b64 s[10:11], s[10:11], 3
	v_or_b32_e32 v38, 0x100, v0
	v_lshl_add_u64 v[10:11], v[6:7], 0, v[34:35]
	v_lshl_add_u64 v[2:3], v[2:3], 0, s[10:11]
	v_lshrrev_b32_e32 v39, 7, v38
	v_lshl_add_u64 v[12:13], v[2:3], 0, v[34:35]
	global_load_dwordx4 v[2:5], v[10:11], off nt
	global_load_dwordx4 v[6:9], v[12:13], off nt
	v_lshl_or_b32 v10, v39, 19, s14
	v_mov_b32_e32 v11, v35
	v_lshl_add_u64 v[10:11], s[8:9], 0, v[10:11]
	v_lshl_add_u64 v[12:13], v[10:11], 0, v[26:27]
	v_lshl_add_u64 v[12:13], v[12:13], 0, s[12:13]
	v_lshl_add_u64 v[10:11], v[10:11], 0, v[28:29]
	v_lshl_add_u64 v[18:19], v[12:13], 0, v[34:35]
	v_lshl_add_u64 v[10:11], v[10:11], 0, s[10:11]
	v_lshl_add_u64 v[20:21], v[10:11], 0, v[34:35]
	global_load_dwordx4 v[10:13], v[18:19], off nt
	global_load_dwordx4 v[14:17], v[20:21], off nt
	v_or_b32_e32 v18, 0x200, v0
	v_lshrrev_b32_e32 v40, 7, v18
	v_lshl_or_b32 v18, v40, 19, s14
	v_mov_b32_e32 v19, v35
	v_lshl_add_u64 v[18:19], s[8:9], 0, v[18:19]
	v_lshl_add_u64 v[20:21], v[18:19], 0, v[26:27]
	v_lshl_add_u64 v[20:21], v[20:21], 0, s[12:13]
	v_lshl_add_u64 v[18:19], v[18:19], 0, v[28:29]
	v_lshl_add_u64 v[30:31], v[20:21], 0, v[34:35]
	v_lshl_add_u64 v[18:19], v[18:19], 0, s[10:11]
	v_lshl_add_u64 v[32:33], v[18:19], 0, v[34:35]
	global_load_dwordx4 v[18:21], v[30:31], off nt
	global_load_dwordx4 v[22:25], v[32:33], off nt
	v_or_b32_e32 v30, 0x300, v0
	v_lshrrev_b32_e32 v41, 7, v30
	v_lshl_or_b32 v30, v41, 19, s14
	v_mov_b32_e32 v31, v35
	v_lshl_add_u64 v[30:31], s[8:9], 0, v[30:31]
	v_lshl_add_u64 v[26:27], v[30:31], 0, v[26:27]
	v_lshl_add_u64 v[30:31], v[30:31], 0, v[28:29]
	v_lshl_add_u64 v[26:27], v[26:27], 0, s[12:13]
	v_lshl_add_u64 v[30:31], v[30:31], 0, s[10:11]
	v_lshl_add_u64 v[26:27], v[26:27], 0, v[34:35]
	v_lshl_add_u64 v[30:31], v[30:31], 0, v[34:35]
	global_load_dwordx4 v[26:29], v[26:27], off nt
	v_mul_u32_u24_e32 v42, 0x88, v1
	global_load_dwordx4 v[30:33], v[30:31], off nt
	v_mul_u32_u24_e32 v37, 0x880, v37
	v_lshlrev_b32_e32 v1, 3, v1
	v_mul_u32_u24_e32 v36, 0x88, v36
	v_mul_u32_u24_e32 v39, 0x880, v39
	v_mul_u32_u24_e32 v40, 0x880, v40
	v_add3_u32 v43, v37, v36, v1
	v_add3_u32 v44, v39, v36, v1
	v_add3_u32 v37, v42, v37, v34
	v_add_u32_e32 v43, 0x4000, v43
	v_add_u32_e32 v44, 0x4000, v44
	v_add3_u32 v39, v42, v39, v34
	v_lshrrev_b32_e32 v35, 3, v0
	s_waitcnt vmcnt(7)
	ds_write2_b64 v37, v[2:3], v[4:5] offset1:1
	s_waitcnt vmcnt(5)
	ds_write2_b64 v39, v[10:11], v[12:13] offset1:1
	ds_write2_b64 v43, v[6:7], v[8:9] offset0:128 offset1:145
	s_waitcnt vmcnt(4)
	ds_write2_b64 v44, v[14:15], v[16:17] offset0:128 offset1:145
	v_add3_u32 v2, v42, v40, v34
	s_waitcnt vmcnt(3)
	ds_write2_b64 v2, v[18:19], v[20:21] offset1:1
	v_add3_u32 v2, v40, v36, v1
	v_add_u32_e32 v2, 0x4000, v2
	s_waitcnt vmcnt(2)
	ds_write2_b64 v2, v[22:23], v[24:25] offset0:128 offset1:145
	v_mul_u32_u24_e32 v2, 0x880, v41
	v_add3_u32 v1, v2, v36, v1
	v_add3_u32 v3, v42, v2, v34
	v_add_u32_e32 v1, 0x4000, v1
	v_bfe_u32 v25, v0, 4, 1
	v_lshlrev_b32_e32 v4, 6, v25
	v_cndmask_b32_e64 v24, 0, 1.0, s[6:7]
	s_lshl_b32 s6, s2, 3
	s_waitcnt vmcnt(1)
	ds_write2_b64 v3, v[26:27], v[28:29] offset1:1
	v_lshrrev_b32_e32 v28, 5, v0
	s_waitcnt vmcnt(0)
	ds_write2_b64 v1, v[30:31], v[32:33] offset0:128 offset1:145
	v_and_b32_e32 v1, 15, v0
	v_mul_u32_u24_e32 v2, 0x880, v28
	v_mul_u32_u24_e32 v3, 0x88, v1
	v_add3_u32 v22, v2, v3, v4
	v_add_u32_e32 v2, 0x4400, v22
	s_waitcnt lgkmcnt(0)
	s_barrier
	ds_read2_b64 v[2:5], v2 offset1:1
	ds_read2_b64 v[6:9], v22 offset1:1
	ds_read2_b64 v[14:17], v22 offset0:2 offset1:3
	v_add_u32_e32 v10, 0x4410, v22
	ds_read2_b64 v[10:13], v10 offset1:1
	s_waitcnt lgkmcnt(3)
	v_mov_b32_e32 v19, v4
	s_waitcnt lgkmcnt(2)
	v_mov_b32_e32 v21, v8
	v_mov_b32_e32 v4, v3
	v_mov_b32_e32 v8, v7
	v_pk_fma_f32 v[4:5], v[24:25], v[4:5], v[8:9] op_sel_hi:[0,1,1] neg_lo:[0,0,1] neg_hi:[0,0,1]
	v_mov_b32_e32 v20, v6
	v_cvt_pk_f16_f32 v6, v4, v5
	s_waitcnt lgkmcnt(0)
	v_mov_b32_e32 v4, v10
	v_mov_b32_e32 v5, v12
	v_mov_b32_e32 v8, v14
	v_mov_b32_e32 v9, v16
	v_pk_fma_f32 v[4:5], v[24:25], v[4:5], v[8:9] op_sel_hi:[0,1,1]
	v_mov_b32_e32 v12, v11
	v_mov_b32_e32 v16, v15
	v_mov_b32_e32 v18, v2
	v_cvt_pk_f16_f32 v3, v4, v5
	v_pk_fma_f32 v[4:5], v[24:25], v[12:13], v[16:17] op_sel_hi:[0,1,1] neg_lo:[0,0,1] neg_hi:[0,0,1]
	v_add_u32_e32 v7, 0x4420, v22
	v_pk_fma_f32 v[18:19], v[24:25], v[18:19], v[20:21] op_sel_hi:[0,1,1]
	ds_read2_b64 v[8:11], v7 offset1:1
	v_cvt_pk_f16_f32 v7, v4, v5
	ds_read2_b64 v[12:15], v22 offset0:4 offset1:5
	v_add_u32_e32 v4, 0x4430, v22
	v_cvt_pk_f16_f32 v2, v18, v19
	ds_read2_b64 v[16:19], v4 offset1:1
	ds_read2_b64 v[20:23], v22 offset0:6 offset1:7
	s_waitcnt lgkmcnt(3)
	v_mov_b32_e32 v5, v10
	s_waitcnt lgkmcnt(2)
	v_mov_b32_e32 v27, v14
	v_mov_b32_e32 v10, v9
	v_mov_b32_e32 v14, v13
	v_mov_b32_e32 v4, v8
	v_mov_b32_e32 v26, v12
	v_pk_fma_f32 v[8:9], v[24:25], v[10:11], v[14:15] op_sel_hi:[0,1,1] neg_lo:[0,0,1] neg_hi:[0,0,1]
	s_waitcnt lgkmcnt(1)
	v_mov_b32_e32 v10, v16
	v_mov_b32_e32 v11, v18
	s_waitcnt lgkmcnt(0)
	v_mov_b32_e32 v12, v20
	v_mov_b32_e32 v13, v22
	v_pk_fma_f32 v[4:5], v[24:25], v[4:5], v[26:27] op_sel_hi:[0,1,1]
	v_pk_fma_f32 v[10:11], v[24:25], v[10:11], v[12:13] op_sel_hi:[0,1,1]
	v_mov_b32_e32 v18, v17
	v_mov_b32_e32 v22, v21
	v_cvt_pk_f16_f32 v4, v4, v5
	v_cvt_pk_f16_f32 v5, v10, v11
	v_pk_fma_f32 v[10:11], v[24:25], v[18:19], v[22:23] op_sel_hi:[0,1,1] neg_lo:[0,0,1] neg_hi:[0,0,1]
	v_cvt_pk_f16_f32 v8, v8, v9
	v_cvt_pk_f16_f32 v9, v10, v11
	v_lshlrev_b32_e32 v1, 9, v1
	v_lshlrev_b32_e32 v10, 7, v25
	v_lshlrev_b32_e32 v11, 4, v28
	v_or3_b32 v1, v1, v10, v11
	v_lshrrev_b32_e32 v29, 4, v0
	ds_write_b128 v1, v[2:5] offset:34816
	ds_write_b128 v1, v[6:9] offset:35072
	v_and_b32_e32 v1, 7, v0
	v_mov_b32_e32 v2, 0x8800
	v_lshl_or_b32 v12, s3, 5, v25
	v_lshlrev_b32_e32 v7, 2, v0
	v_lshl_or_b32 v8, v1, 4, v2
	s_lshl_b32 s3, s2, 4
	v_and_or_b32 v6, v29, 14, v12
	v_and_b32_e32 v13, 32, v7
	s_and_b32 s3, s3, 64
	v_and_or_b32 v1, s6, 24, v1
	v_lshl_add_u32 v2, v35, 7, v8
	v_lshl_or_b32 v6, v6, 7, v13
	s_waitcnt lgkmcnt(0)
	s_barrier
	ds_read_b128 v[2:5], v2
	v_or3_b32 v6, v6, s3, v1
	v_ashrrev_i32_e32 v7, 31, v6
	v_lshl_add_u64 v[10:11], v[6:7], 4, s[4:5]
	v_lshlrev_b32_e32 v6, 4, v38
	v_and_b32_e32 v6, 0x1f80, v6
	v_add_u32_e32 v6, v8, v6
	ds_read_b128 v[6:9], v6
	s_waitcnt lgkmcnt(1)
	global_store_dwordx4 v[10:11], v[2:5], off sc0 sc1
	s_nop 1
	v_lshrrev_b32_e32 v2, 4, v38
	v_and_or_b32 v2, v2, 30, v12
	v_lshl_or_b32 v2, v2, 7, v13
	v_or3_b32 v2, v2, s3, v1
	v_ashrrev_i32_e32 v3, 31, v2
	v_lshl_add_u64 v[2:3], v[2:3], 4, s[4:5]
	s_waitcnt lgkmcnt(0)
	global_store_dwordx4 v[2:3], v[6:9], off sc0 sc1
	s_branch .LBB0_2

_Z9feat_gemmPKDF16_S0_PDF16_:
	s_load_dwordx4 s[4:7], s[0:1], 0x8
	s_load_dwordx2 s[8:9], s[0:1], 0x0
	s_lshr_b32 s10, s2, 6
	s_lshl_b32 s10, s10, 3
	s_and_b32 s11, s2, 7
	s_or_b32 s10, s10, s11
	s_bfe_u32 s11, s2, 0x30003
	s_mul_i32 s12, s10, 0x44
	s_lshr_b32 s14, s12, 4
	s_lshl_b32 s15, s14, 3
	s_sub_u32 s15, 0x441, s15
	v_cvt_f32_u32_e32 v174, s15
	v_sqrt_f32_e32 v174, v174
	v_and_b32_e32 v170, 63, v0
	v_lshrrev_b32_e32 v171, 6, v0
	v_sub_f32_e32 v174, 0x42040000, v174
	v_fmaak_f32 v174, 0.5, v174, 0x3c23d70a
	v_cvt_u32_f32_e32 v174, v174
	v_lshlrev_b32_e32 v160, 4, v170
	v_readfirstlane_b32 s13, v174
	s_sub_u32 s15, 33, s13
	s_mul_i32 s15, s15, s13
	s_lshr_b32 s15, s15, 1
	s_sub_u32 s14, s14, s15
	s_add_u32 s14, s14, s13
	s_bfe_u32 s46, s12, 0x20002
	v_and_b32_e32 v172, 31, v170
	v_readfirstlane_b32 s33, v171
	v_lshrrev_b32_e32 v173, 5, v170
	s_lshl_b32 s35, s33, 11
	s_lshl_b32 s34, s11, 8
	s_lshl_b32 s36, s33, 5
	s_add_u32 s34, s34, s36
	v_add_lshl_u32 v165, v172, s34, 4
	v_add_u32_e32 v166, 0x8000, v165
	v_lshl_add_u32 v164, v173, 15, v165
	v_add_u32_e32 v168, s35, v160
	v_mov_b32_e32 v161, v160
	s_waitcnt lgkmcnt(0)
	s_lshl_b32 s36, s12, 12
	s_add_u32 s20, s4, s36
	s_addc_u32 s21, s5, 0
	s_min_u32 s43, s13, 15
	s_min_u32 s44, s14, 15
	s_lshl_b32 s45, s44, 16
	s_add_u32 s24, s8, s45
	s_addc_u32 s25, s9, 0
	s_add_u32 s26, s24, 0x100000
	s_addc_u32 s27, s25, 0
	s_lshl_b32 s45, s43, 16
	s_add_u32 s28, s8, s45
	s_addc_u32 s29, s9, 0
	s_add_u32 s30, s28, 0x100000
	s_addc_u32 s31, s29, 0
	global_load_dwordx4 v[36:39], v164, s[24:25]
	global_load_dwordx4 v[32:35], v164, s[26:27]
	global_load_dwordx4 v[40:43], v165, s[28:29]
	global_load_dwordx4 v[44:47], v166, s[28:29]
	global_load_dwordx4 v[48:51], v165, s[30:31]
	global_load_dwordx4 v[52:55], v166, s[30:31]
	s_mov_b32 s17, 0
	s_mov_b32 s18, 0
	s_mov_b32 s19, 0
	s_mov_b32 s22, 0
	s_sub_u32 s39, 5, s46
	s_mov_b32 s38, 0

.Lk2_epi:
	s_waitcnt vmcnt(0) lgkmcnt(0)
	s_nop 15
	s_barrier
	v_lshlrev_b32_e32 v180, 12, v171
	v_lshlrev_b32_e32 v181, 6, v172
	v_lshlrev_b32_e32 v182, 3, v173
	v_or3_b32 v181, v180, v181, v182
	v_add_u32_e32 v182, 0x800, v181
	v_cvt_pk_f16_f32 v184, v16, v17
	v_cvt_pk_f16_f32 v185, v18, v19
	v_cvt_pk_f16_f32 v186, v20, v21
	v_cvt_pk_f16_f32 v187, v22, v23
	v_cvt_pk_f16_f32 v188, v24, v25
	v_cvt_pk_f16_f32 v189, v26, v27
	v_cvt_pk_f16_f32 v190, v28, v29
	v_cvt_pk_f16_f32 v191, v30, v31
	ds_write2_b64 v181, v[184:185], v[186:187] offset1:2
	ds_write2_b64 v181, v[188:189], v[190:191] offset0:4 offset1:6
	v_cvt_pk_f16_f32 v184, v0, v1
	v_cvt_pk_f16_f32 v185, v2, v3
	v_cvt_pk_f16_f32 v186, v4, v5
	v_cvt_pk_f16_f32 v187, v6, v7
	v_cvt_pk_f16_f32 v188, v8, v9
	v_cvt_pk_f16_f32 v189, v10, v11
	v_cvt_pk_f16_f32 v190, v12, v13
	v_cvt_pk_f16_f32 v191, v14, v15
	ds_write2_b64 v182, v[184:185], v[186:187] offset1:2
	ds_write2_b64 v182, v[188:189], v[190:191] offset0:4 offset1:6
	s_lshl_b32 s36, s10, 18
	s_add_u32 s0, s6, s36
	s_addc_u32 s1, s7, 0
	s_lshl_b32 s36, s11, 3
	s_add_u32 s36, s36, s33
	s_lshl_b32 s36, s36, 12
	s_add_u32 s0, s0, s36
	s_addc_u32 s1, s1, 0
	v_or_b32_e32 v183, v180, v160
	s_waitcnt lgkmcnt(0)
	ds_read_b128 v[0:3], v183
	ds_read_b128 v[4:7], v183 offset:1024
	ds_read_b128 v[8:11], v183 offset:2048
	ds_read_b128 v[12:15], v183 offset:3072
	s_waitcnt lgkmcnt(3)
	global_store_dwordx4 v160, v[0:3], s[0:1] sc0 sc1
	s_waitcnt lgkmcnt(2)
	global_store_dwordx4 v160, v[4:7], s[0:1] offset:1024 sc0 sc1
	s_waitcnt lgkmcnt(1)
	global_store_dwordx4 v160, v[8:11], s[0:1] offset:2048 sc0 sc1
	s_waitcnt lgkmcnt(0)
	global_store_dwordx4 v160, v[12:15], s[0:1] offset:3072 sc0 sc1
	s_endpgm

_Z13reduce_kernelPKDF16_Pf:
	s_load_dwordx4 s[4:7], s[0:1], 0x0
	v_lshl_or_b32 v2, s2, 8, v0
	v_lshlrev_b32_e32 v1, 3, v2
	v_mov_b32_e32 v6, 0
	v_mov_b32_e32 v7, 0
	v_mov_b32_e32 v8, 0
	v_mov_b32_e32 v9, 0
	s_waitcnt lgkmcnt(0)
	global_load_dwordx2 v[10:11], v1, s[4:5] nt
	s_add_u32 s4, s4, 0x40000
	s_addc_u32 s5, s5, 0
	global_load_dwordx2 v[12:13], v1, s[4:5] nt
	s_add_u32 s4, s4, 0x40000
	s_addc_u32 s5, s5, 0
	global_load_dwordx2 v[14:15], v1, s[4:5] nt
	s_add_u32 s4, s4, 0x40000
	s_addc_u32 s5, s5, 0
	global_load_dwordx2 v[16:17], v1, s[4:5] nt
	s_add_u32 s4, s4, 0x40000
	s_addc_u32 s5, s5, 0
	global_load_dwordx2 v[18:19], v1, s[4:5] nt
	s_add_u32 s4, s4, 0x40000
	s_addc_u32 s5, s5, 0
	global_load_dwordx2 v[20:21], v1, s[4:5] nt
	s_add_u32 s4, s4, 0x40000
	s_addc_u32 s5, s5, 0
	global_load_dwordx2 v[22:23], v1, s[4:5] nt
	s_add_u32 s4, s4, 0x40000
	s_addc_u32 s5, s5, 0
	global_load_dwordx2 v[24:25], v1, s[4:5] nt
	s_add_u32 s4, s4, 0x40000
	s_addc_u32 s5, s5, 0
	global_load_dwordx2 v[26:27], v1, s[4:5] nt
	s_add_u32 s4, s4, 0x40000
	s_addc_u32 s5, s5, 0
	global_load_dwordx2 v[28:29], v1, s[4:5] nt
	s_add_u32 s4, s4, 0x40000
	s_addc_u32 s5, s5, 0
	global_load_dwordx2 v[30:31], v1, s[4:5] nt
	s_add_u32 s4, s4, 0x40000
	s_addc_u32 s5, s5, 0
	global_load_dwordx2 v[32:33], v1, s[4:5] nt
	s_add_u32 s4, s4, 0x40000
	s_addc_u32 s5, s5, 0
	global_load_dwordx2 v[34:35], v1, s[4:5] nt
	s_add_u32 s4, s4, 0x40000
	s_addc_u32 s5, s5, 0
	global_load_dwordx2 v[36:37], v1, s[4:5] nt
	s_add_u32 s4, s4, 0x40000
	s_addc_u32 s5, s5, 0
	global_load_dwordx2 v[38:39], v1, s[4:5] nt
	s_add_u32 s4, s4, 0x40000
	s_addc_u32 s5, s5, 0
	global_load_dwordx2 v[40:41], v1, s[4:5] nt
	s_add_u32 s4, s4, 0x40000
	s_addc_u32 s5, s5, 0
	global_load_dwordx2 v[42:43], v1, s[4:5] nt
	s_add_u32 s4, s4, 0x40000
	s_addc_u32 s5, s5, 0
	global_load_dwordx2 v[44:45], v1, s[4:5] nt
	s_add_u32 s4, s4, 0x40000
	s_addc_u32 s5, s5, 0
	global_load_dwordx2 v[46:47], v1, s[4:5] nt
	s_add_u32 s4, s4, 0x40000
	s_addc_u32 s5, s5, 0
	global_load_dwordx2 v[48:49], v1, s[4:5] nt
	s_add_u32 s4, s4, 0x40000
	s_addc_u32 s5, s5, 0
	global_load_dwordx2 v[50:51], v1, s[4:5] nt
	s_add_u32 s4, s4, 0x40000
	s_addc_u32 s5, s5, 0
	global_load_dwordx2 v[52:53], v1, s[4:5] nt
	s_add_u32 s4, s4, 0x40000
	s_addc_u32 s5, s5, 0
	global_load_dwordx2 v[54:55], v1, s[4:5] nt
	s_add_u32 s4, s4, 0x40000
	s_addc_u32 s5, s5, 0
	global_load_dwordx2 v[56:57], v1, s[4:5] nt
	s_add_u32 s4, s4, 0x40000
	s_addc_u32 s5, s5, 0
	global_load_dwordx2 v[58:59], v1, s[4:5] nt
	s_add_u32 s4, s4, 0x40000
	s_addc_u32 s5, s5, 0
	global_load_dwordx2 v[60:61], v1, s[4:5] nt
	s_add_u32 s4, s4, 0x40000
	s_addc_u32 s5, s5, 0
	global_load_dwordx2 v[62:63], v1, s[4:5] nt
	s_add_u32 s4, s4, 0x40000
	s_addc_u32 s5, s5, 0
	global_load_dwordx2 v[64:65], v1, s[4:5] nt
	s_add_u32 s4, s4, 0x40000
	s_addc_u32 s5, s5, 0
	global_load_dwordx2 v[66:67], v1, s[4:5] nt
	s_add_u32 s4, s4, 0x40000
	s_addc_u32 s5, s5, 0
	global_load_dwordx2 v[68:69], v1, s[4:5] nt
	s_add_u32 s4, s4, 0x40000
	s_addc_u32 s5, s5, 0
	global_load_dwordx2 v[70:71], v1, s[4:5] nt
	s_add_u32 s4, s4, 0x40000
	s_addc_u32 s5, s5, 0
	global_load_dwordx2 v[72:73], v1, s[4:5] nt
	s_waitcnt vmcnt(31)
	v_cvt_f32_f16_e32 v74, v10
	v_cvt_f32_f16_sdwa v75, v10 dst_sel:DWORD dst_unused:UNUSED_PAD src0_sel:WORD_1
	v_cvt_f32_f16_e32 v76, v11
	v_cvt_f32_f16_sdwa v77, v11 dst_sel:DWORD dst_unused:UNUSED_PAD src0_sel:WORD_1
	v_pk_add_f32 v[6:7], v[6:7], v[74:75]
	v_pk_add_f32 v[8:9], v[8:9], v[76:77]
	s_waitcnt vmcnt(30)
	v_cvt_f32_f16_e32 v74, v12
	v_cvt_f32_f16_sdwa v75, v12 dst_sel:DWORD dst_unused:UNUSED_PAD src0_sel:WORD_1
	v_cvt_f32_f16_e32 v76, v13
	v_cvt_f32_f16_sdwa v77, v13 dst_sel:DWORD dst_unused:UNUSED_PAD src0_sel:WORD_1
	v_pk_add_f32 v[6:7], v[6:7], v[74:75]
	v_pk_add_f32 v[8:9], v[8:9], v[76:77]
	s_waitcnt vmcnt(29)
	v_cvt_f32_f16_e32 v74, v14
	v_cvt_f32_f16_sdwa v75, v14 dst_sel:DWORD dst_unused:UNUSED_PAD src0_sel:WORD_1
	v_cvt_f32_f16_e32 v76, v15
	v_cvt_f32_f16_sdwa v77, v15 dst_sel:DWORD dst_unused:UNUSED_PAD src0_sel:WORD_1
	v_pk_add_f32 v[6:7], v[6:7], v[74:75]
	v_pk_add_f32 v[8:9], v[8:9], v[76:77]
	s_waitcnt vmcnt(28)
	v_cvt_f32_f16_e32 v74, v16
	v_cvt_f32_f16_sdwa v75, v16 dst_sel:DWORD dst_unused:UNUSED_PAD src0_sel:WORD_1
	v_cvt_f32_f16_e32 v76, v17
	v_cvt_f32_f16_sdwa v77, v17 dst_sel:DWORD dst_unused:UNUSED_PAD src0_sel:WORD_1
	v_pk_add_f32 v[6:7], v[6:7], v[74:75]
	v_pk_add_f32 v[8:9], v[8:9], v[76:77]
	s_waitcnt vmcnt(27)
	v_cvt_f32_f16_e32 v74, v18
	v_cvt_f32_f16_sdwa v75, v18 dst_sel:DWORD dst_unused:UNUSED_PAD src0_sel:WORD_1
	v_cvt_f32_f16_e32 v76, v19
	v_cvt_f32_f16_sdwa v77, v19 dst_sel:DWORD dst_unused:UNUSED_PAD src0_sel:WORD_1
	v_pk_add_f32 v[6:7], v[6:7], v[74:75]
	v_pk_add_f32 v[8:9], v[8:9], v[76:77]
	s_waitcnt vmcnt(26)
	v_cvt_f32_f16_e32 v74, v20
	v_cvt_f32_f16_sdwa v75, v20 dst_sel:DWORD dst_unused:UNUSED_PAD src0_sel:WORD_1
	v_cvt_f32_f16_e32 v76, v21
	v_cvt_f32_f16_sdwa v77, v21 dst_sel:DWORD dst_unused:UNUSED_PAD src0_sel:WORD_1
	v_pk_add_f32 v[6:7], v[6:7], v[74:75]
	v_pk_add_f32 v[8:9], v[8:9], v[76:77]
	s_waitcnt vmcnt(25)
	v_cvt_f32_f16_e32 v74, v22
	v_cvt_f32_f16_sdwa v75, v22 dst_sel:DWORD dst_unused:UNUSED_PAD src0_sel:WORD_1
	v_cvt_f32_f16_e32 v76, v23
	v_cvt_f32_f16_sdwa v77, v23 dst_sel:DWORD dst_unused:UNUSED_PAD src0_sel:WORD_1
	v_pk_add_f32 v[6:7], v[6:7], v[74:75]
	v_pk_add_f32 v[8:9], v[8:9], v[76:77]
	s_waitcnt vmcnt(24)
	v_cvt_f32_f16_e32 v74, v24
	v_cvt_f32_f16_sdwa v75, v24 dst_sel:DWORD dst_unused:UNUSED_PAD src0_sel:WORD_1
	v_cvt_f32_f16_e32 v76, v25
	v_cvt_f32_f16_sdwa v77, v25 dst_sel:DWORD dst_unused:UNUSED_PAD src0_sel:WORD_1
	v_pk_add_f32 v[6:7], v[6:7], v[74:75]
	v_pk_add_f32 v[8:9], v[8:9], v[76:77]
	s_waitcnt vmcnt(23)
	v_cvt_f32_f16_e32 v74, v26
	v_cvt_f32_f16_sdwa v75, v26 dst_sel:DWORD dst_unused:UNUSED_PAD src0_sel:WORD_1
	v_cvt_f32_f16_e32 v76, v27
	v_cvt_f32_f16_sdwa v77, v27 dst_sel:DWORD dst_unused:UNUSED_PAD src0_sel:WORD_1
	v_pk_add_f32 v[6:7], v[6:7], v[74:75]
	v_pk_add_f32 v[8:9], v[8:9], v[76:77]
	s_waitcnt vmcnt(22)
	v_cvt_f32_f16_e32 v74, v28
	v_cvt_f32_f16_sdwa v75, v28 dst_sel:DWORD dst_unused:UNUSED_PAD src0_sel:WORD_1
	v_cvt_f32_f16_e32 v76, v29
	v_cvt_f32_f16_sdwa v77, v29 dst_sel:DWORD dst_unused:UNUSED_PAD src0_sel:WORD_1
	v_pk_add_f32 v[6:7], v[6:7], v[74:75]
	v_pk_add_f32 v[8:9], v[8:9], v[76:77]
	s_waitcnt vmcnt(21)
	v_cvt_f32_f16_e32 v74, v30
	v_cvt_f32_f16_sdwa v75, v30 dst_sel:DWORD dst_unused:UNUSED_PAD src0_sel:WORD_1
	v_cvt_f32_f16_e32 v76, v31
	v_cvt_f32_f16_sdwa v77, v31 dst_sel:DWORD dst_unused:UNUSED_PAD src0_sel:WORD_1
	v_pk_add_f32 v[6:7], v[6:7], v[74:75]
	v_pk_add_f32 v[8:9], v[8:9], v[76:77]
	s_waitcnt vmcnt(20)
	v_cvt_f32_f16_e32 v74, v32
	v_cvt_f32_f16_sdwa v75, v32 dst_sel:DWORD dst_unused:UNUSED_PAD src0_sel:WORD_1
	v_cvt_f32_f16_e32 v76, v33
	v_cvt_f32_f16_sdwa v77, v33 dst_sel:DWORD dst_unused:UNUSED_PAD src0_sel:WORD_1
	v_pk_add_f32 v[6:7], v[6:7], v[74:75]
	v_pk_add_f32 v[8:9], v[8:9], v[76:77]
	s_waitcnt vmcnt(19)
	v_cvt_f32_f16_e32 v74, v34
	v_cvt_f32_f16_sdwa v75, v34 dst_sel:DWORD dst_unused:UNUSED_PAD src0_sel:WORD_1
	v_cvt_f32_f16_e32 v76, v35
	v_cvt_f32_f16_sdwa v77, v35 dst_sel:DWORD dst_unused:UNUSED_PAD src0_sel:WORD_1
	v_pk_add_f32 v[6:7], v[6:7], v[74:75]
	v_pk_add_f32 v[8:9], v[8:9], v[76:77]
	s_waitcnt vmcnt(18)
	v_cvt_f32_f16_e32 v74, v36
	v_cvt_f32_f16_sdwa v75, v36 dst_sel:DWORD dst_unused:UNUSED_PAD src0_sel:WORD_1
	v_cvt_f32_f16_e32 v76, v37
	v_cvt_f32_f16_sdwa v77, v37 dst_sel:DWORD dst_unused:UNUSED_PAD src0_sel:WORD_1
	v_pk_add_f32 v[6:7], v[6:7], v[74:75]
	v_pk_add_f32 v[8:9], v[8:9], v[76:77]
	s_waitcnt vmcnt(17)
	v_cvt_f32_f16_e32 v74, v38
	v_cvt_f32_f16_sdwa v75, v38 dst_sel:DWORD dst_unused:UNUSED_PAD src0_sel:WORD_1
	v_cvt_f32_f16_e32 v76, v39
	v_cvt_f32_f16_sdwa v77, v39 dst_sel:DWORD dst_unused:UNUSED_PAD src0_sel:WORD_1
	v_pk_add_f32 v[6:7], v[6:7], v[74:75]
	v_pk_add_f32 v[8:9], v[8:9], v[76:77]
	s_waitcnt vmcnt(16)
	v_cvt_f32_f16_e32 v74, v40
	v_cvt_f32_f16_sdwa v75, v40 dst_sel:DWORD dst_unused:UNUSED_PAD src0_sel:WORD_1
	v_cvt_f32_f16_e32 v76, v41
	v_cvt_f32_f16_sdwa v77, v41 dst_sel:DWORD dst_unused:UNUSED_PAD src0_sel:WORD_1
	v_pk_add_f32 v[6:7], v[6:7], v[74:75]
	v_pk_add_f32 v[8:9], v[8:9], v[76:77]
	s_waitcnt vmcnt(15)
	v_cvt_f32_f16_e32 v74, v42
	v_cvt_f32_f16_sdwa v75, v42 dst_sel:DWORD dst_unused:UNUSED_PAD src0_sel:WORD_1
	v_cvt_f32_f16_e32 v76, v43
	v_cvt_f32_f16_sdwa v77, v43 dst_sel:DWORD dst_unused:UNUSED_PAD src0_sel:WORD_1
	v_pk_add_f32 v[6:7], v[6:7], v[74:75]
	v_pk_add_f32 v[8:9], v[8:9], v[76:77]
	s_waitcnt vmcnt(14)
	v_cvt_f32_f16_e32 v74, v44
	v_cvt_f32_f16_sdwa v75, v44 dst_sel:DWORD dst_unused:UNUSED_PAD src0_sel:WORD_1
	v_cvt_f32_f16_e32 v76, v45
	v_cvt_f32_f16_sdwa v77, v45 dst_sel:DWORD dst_unused:UNUSED_PAD src0_sel:WORD_1
	v_pk_add_f32 v[6:7], v[6:7], v[74:75]
	v_pk_add_f32 v[8:9], v[8:9], v[76:77]
	s_waitcnt vmcnt(13)
	v_cvt_f32_f16_e32 v74, v46
	v_cvt_f32_f16_sdwa v75, v46 dst_sel:DWORD dst_unused:UNUSED_PAD src0_sel:WORD_1
	v_cvt_f32_f16_e32 v76, v47
	v_cvt_f32_f16_sdwa v77, v47 dst_sel:DWORD dst_unused:UNUSED_PAD src0_sel:WORD_1
	v_pk_add_f32 v[6:7], v[6:7], v[74:75]
	v_pk_add_f32 v[8:9], v[8:9], v[76:77]
	s_waitcnt vmcnt(12)
	v_cvt_f32_f16_e32 v74, v48
	v_cvt_f32_f16_sdwa v75, v48 dst_sel:DWORD dst_unused:UNUSED_PAD src0_sel:WORD_1
	v_cvt_f32_f16_e32 v76, v49
	v_cvt_f32_f16_sdwa v77, v49 dst_sel:DWORD dst_unused:UNUSED_PAD src0_sel:WORD_1
	v_pk_add_f32 v[6:7], v[6:7], v[74:75]
	v_pk_add_f32 v[8:9], v[8:9], v[76:77]
	s_waitcnt vmcnt(11)
	v_cvt_f32_f16_e32 v74, v50
	v_cvt_f32_f16_sdwa v75, v50 dst_sel:DWORD dst_unused:UNUSED_PAD src0_sel:WORD_1
	v_cvt_f32_f16_e32 v76, v51
	v_cvt_f32_f16_sdwa v77, v51 dst_sel:DWORD dst_unused:UNUSED_PAD src0_sel:WORD_1
	v_pk_add_f32 v[6:7], v[6:7], v[74:75]
	v_pk_add_f32 v[8:9], v[8:9], v[76:77]
	s_waitcnt vmcnt(10)
	v_cvt_f32_f16_e32 v74, v52
	v_cvt_f32_f16_sdwa v75, v52 dst_sel:DWORD dst_unused:UNUSED_PAD src0_sel:WORD_1
	v_cvt_f32_f16_e32 v76, v53
	v_cvt_f32_f16_sdwa v77, v53 dst_sel:DWORD dst_unused:UNUSED_PAD src0_sel:WORD_1
	v_pk_add_f32 v[6:7], v[6:7], v[74:75]
	v_pk_add_f32 v[8:9], v[8:9], v[76:77]
	s_waitcnt vmcnt(9)
	v_cvt_f32_f16_e32 v74, v54
	v_cvt_f32_f16_sdwa v75, v54 dst_sel:DWORD dst_unused:UNUSED_PAD src0_sel:WORD_1
	v_cvt_f32_f16_e32 v76, v55
	v_cvt_f32_f16_sdwa v77, v55 dst_sel:DWORD dst_unused:UNUSED_PAD src0_sel:WORD_1
	v_pk_add_f32 v[6:7], v[6:7], v[74:75]
	v_pk_add_f32 v[8:9], v[8:9], v[76:77]
	s_waitcnt vmcnt(8)
	v_cvt_f32_f16_e32 v74, v56
	v_cvt_f32_f16_sdwa v75, v56 dst_sel:DWORD dst_unused:UNUSED_PAD src0_sel:WORD_1
	v_cvt_f32_f16_e32 v76, v57
	v_cvt_f32_f16_sdwa v77, v57 dst_sel:DWORD dst_unused:UNUSED_PAD src0_sel:WORD_1
	v_pk_add_f32 v[6:7], v[6:7], v[74:75]
	v_pk_add_f32 v[8:9], v[8:9], v[76:77]
	s_waitcnt vmcnt(7)
	v_cvt_f32_f16_e32 v74, v58
	v_cvt_f32_f16_sdwa v75, v58 dst_sel:DWORD dst_unused:UNUSED_PAD src0_sel:WORD_1
	v_cvt_f32_f16_e32 v76, v59
	v_cvt_f32_f16_sdwa v77, v59 dst_sel:DWORD dst_unused:UNUSED_PAD src0_sel:WORD_1
	v_pk_add_f32 v[6:7], v[6:7], v[74:75]
	v_pk_add_f32 v[8:9], v[8:9], v[76:77]
	s_waitcnt vmcnt(6)
	v_cvt_f32_f16_e32 v74, v60
	v_cvt_f32_f16_sdwa v75, v60 dst_sel:DWORD dst_unused:UNUSED_PAD src0_sel:WORD_1
	v_cvt_f32_f16_e32 v76, v61
	v_cvt_f32_f16_sdwa v77, v61 dst_sel:DWORD dst_unused:UNUSED_PAD src0_sel:WORD_1
	v_pk_add_f32 v[6:7], v[6:7], v[74:75]
	v_pk_add_f32 v[8:9], v[8:9], v[76:77]
	s_waitcnt vmcnt(5)
	v_cvt_f32_f16_e32 v74, v62
	v_cvt_f32_f16_sdwa v75, v62 dst_sel:DWORD dst_unused:UNUSED_PAD src0_sel:WORD_1
	v_cvt_f32_f16_e32 v76, v63
	v_cvt_f32_f16_sdwa v77, v63 dst_sel:DWORD dst_unused:UNUSED_PAD src0_sel:WORD_1
	v_pk_add_f32 v[6:7], v[6:7], v[74:75]
	v_pk_add_f32 v[8:9], v[8:9], v[76:77]
	s_waitcnt vmcnt(4)
	v_cvt_f32_f16_e32 v74, v64
	v_cvt_f32_f16_sdwa v75, v64 dst_sel:DWORD dst_unused:UNUSED_PAD src0_sel:WORD_1
	v_cvt_f32_f16_e32 v76, v65
	v_cvt_f32_f16_sdwa v77, v65 dst_sel:DWORD dst_unused:UNUSED_PAD src0_sel:WORD_1
	v_pk_add_f32 v[6:7], v[6:7], v[74:75]
	v_pk_add_f32 v[8:9], v[8:9], v[76:77]
	s_waitcnt vmcnt(3)
	v_cvt_f32_f16_e32 v74, v66
	v_cvt_f32_f16_sdwa v75, v66 dst_sel:DWORD dst_unused:UNUSED_PAD src0_sel:WORD_1
	v_cvt_f32_f16_e32 v76, v67
	v_cvt_f32_f16_sdwa v77, v67 dst_sel:DWORD dst_unused:UNUSED_PAD src0_sel:WORD_1
	v_pk_add_f32 v[6:7], v[6:7], v[74:75]
	v_pk_add_f32 v[8:9], v[8:9], v[76:77]
	s_waitcnt vmcnt(2)
	v_cvt_f32_f16_e32 v74, v68
	v_cvt_f32_f16_sdwa v75, v68 dst_sel:DWORD dst_unused:UNUSED_PAD src0_sel:WORD_1
	v_cvt_f32_f16_e32 v76, v69
	v_cvt_f32_f16_sdwa v77, v69 dst_sel:DWORD dst_unused:UNUSED_PAD src0_sel:WORD_1
	v_pk_add_f32 v[6:7], v[6:7], v[74:75]
	v_pk_add_f32 v[8:9], v[8:9], v[76:77]
	s_waitcnt vmcnt(1)
	v_cvt_f32_f16_e32 v74, v70
	v_cvt_f32_f16_sdwa v75, v70 dst_sel:DWORD dst_unused:UNUSED_PAD src0_sel:WORD_1
	v_cvt_f32_f16_e32 v76, v71
	v_cvt_f32_f16_sdwa v77, v71 dst_sel:DWORD dst_unused:UNUSED_PAD src0_sel:WORD_1
	v_pk_add_f32 v[6:7], v[6:7], v[74:75]
	v_pk_add_f32 v[8:9], v[8:9], v[76:77]
	s_waitcnt vmcnt(0)
	v_cvt_f32_f16_e32 v74, v72
	v_cvt_f32_f16_sdwa v75, v72 dst_sel:DWORD dst_unused:UNUSED_PAD src0_sel:WORD_1
	v_cvt_f32_f16_e32 v76, v73
	v_cvt_f32_f16_sdwa v77, v73 dst_sel:DWORD dst_unused:UNUSED_PAD src0_sel:WORD_1
	v_pk_add_f32 v[6:7], v[6:7], v[74:75]
	v_pk_add_f32 v[8:9], v[8:9], v[76:77]
	v_lshlrev_b32_e32 v0, 2, v0
	v_ashrrev_i32_e32 v1, 4, v2
	v_and_b32_e32 v0, 28, v0
	s_movk_i32 s0, 0xffe0
	v_and_or_b32 v0, v1, s0, v0
	v_ashrrev_i32_e32 v1, 31, v0
	v_lshlrev_b64 v[0:1], 8, v[0:1]
	v_lshrrev_b32_e32 v2, 1, v2
	v_lshl_add_u64 v[0:1], s[6:7], 0, v[0:1]
	v_and_b32_e32 v2, 0xfc, v2
	v_mov_b32_e32 v3, 0
	v_lshl_add_u64 v[0:1], v[0:1], 0, v[2:3]
	v_mul_f32_e32 v2, 0x3b800000, v6
	global_store_dword v[0:1], v2, off
	v_mul_f32_e32 v2, 0x3b800000, v7
	global_store_dword v[0:1], v2, off offset:256
	v_mul_f32_e32 v2, 0x3b800000, v8
	global_store_dword v[0:1], v2, off offset:512
	v_mul_f32_e32 v2, 0x3b800000, v9
	global_store_dword v[0:1], v2, off offset:768
	s_endpgm

	.amdhsa_kernel _Z13reduce_kernelPKDF16_Pf
		.amdhsa_group_segment_fixed_size 0
		.amdhsa_private_segment_fixed_size 0
		.amdhsa_kernarg_size 16
		.amdhsa_user_sgpr_count 2
		.amdhsa_user_sgpr_dispatch_ptr 0
		.amdhsa_user_sgpr_queue_ptr 0
		.amdhsa_user_sgpr_kernarg_segment_ptr 1
		.amdhsa_user_sgpr_dispatch_id 0
		.amdhsa_user_sgpr_kernarg_preload_length 0
		.amdhsa_user_sgpr_kernarg_preload_offset 0
		.amdhsa_user_sgpr_private_segment_size 0
		.amdhsa_uses_dynamic_stack 0
		.amdhsa_enable_private_segment 0
		.amdhsa_system_sgpr_workgroup_id_x 1
		.amdhsa_system_sgpr_workgroup_id_y 0
		.amdhsa_system_sgpr_workgroup_id_z 0
		.amdhsa_system_sgpr_workgroup_info 0
		.amdhsa_system_vgpr_workitem_id 0
		.amdhsa_next_free_vgpr 78
		.amdhsa_next_free_sgpr 19
		.amdhsa_accum_offset 80
		.amdhsa_reserve_vcc 1
		.amdhsa_float_round_mode_32 0
		.amdhsa_float_round_mode_16_64 0
		.amdhsa_float_denorm_mode_32 3
		.amdhsa_float_denorm_mode_16_64 3
		.amdhsa_dx10_clamp 1
		.amdhsa_ieee_mode 1
		.amdhsa_fp16_overflow 0
		.amdhsa_tg_split 0
		.amdhsa_exception_fp_ieee_invalid_op 0
		.amdhsa_exception_fp_denorm_src 0
		.amdhsa_exception_fp_ieee_div_zero 0
		.amdhsa_exception_fp_ieee_overflow 0
		.amdhsa_exception_fp_ieee_underflow 0
		.amdhsa_exception_fp_ieee_inexact 0
		.amdhsa_exception_int_div_zero 0
	.end_amdhsa_kernel

amdhsa.kernels:
  - .agpr_count:     0
    .args:
      - .actual_access:  read_only
        .address_space:  global
        .offset:         0
        .size:           8
        .value_kind:     global_buffer
      - .actual_access:  read_only
        .address_space:  global
        .offset:         8
        .size:           8
        .value_kind:     global_buffer
      - .actual_access:  write_only
        .address_space:  global
        .offset:         16
        .size:           8
        .value_kind:     global_buffer
      - .actual_access:  read_only
        .address_space:  global
        .offset:         24
        .size:           8
        .value_kind:     global_buffer
      - .actual_access:  write_only
        .address_space:  global
        .offset:         32
        .size:           8
        .value_kind:     global_buffer
    .group_segment_fixed_size: 43008
    .kernarg_segment_align: 8
    .kernarg_segment_size: 40
    .language:       OpenCL C
    .language_version:
      - 2
      - 0
    .max_flat_workgroup_size: 256
    .name:           _Z15sim_prep_kernelPKfS0_PDF16_S0_S1_
    .private_segment_fixed_size: 0
    .sgpr_count:     43
    .sgpr_spill_count: 0
    .symbol:         _Z15sim_prep_kernelPKfS0_PDF16_S0_S1_.kd
    .uniform_work_group_size: 1
    .uses_dynamic_stack: false
    .vgpr_count:     124
    .vgpr_spill_count: 0
    .wavefront_size: 64
  - .agpr_count:     0
    .args:
      - .address_space:  global
        .offset:         0
        .size:           8
        .value_kind:     global_buffer
      - .address_space:  global
        .offset:         8
        .size:           8
        .value_kind:     global_buffer
      - .actual_access:  write_only
        .address_space:  global
        .offset:         16
        .size:           8
        .value_kind:     global_buffer
    .group_segment_fixed_size: 114688
    .kernarg_segment_align: 8
    .kernarg_segment_size: 24
    .language:       OpenCL C
    .language_version:
      - 2
      - 0
    .max_flat_workgroup_size: 512
    .name:           _Z9feat_gemmPKDF16_S0_PDF16_
    .private_segment_fixed_size: 0
    .sgpr_count:     53
    .sgpr_spill_count: 0
    .symbol:         _Z9feat_gemmPKDF16_S0_PDF16_.kd
    .uniform_work_group_size: 1
    .uses_dynamic_stack: false
    .vgpr_count:     192
    .vgpr_spill_count: 0
    .wavefront_size: 64
  - .agpr_count:     0
    .args:
      - .actual_access:  read_only
        .address_space:  global
        .offset:         0
        .size:           8
        .value_kind:     global_buffer
      - .actual_access:  write_only
        .address_space:  global
        .offset:         8
        .size:           8
        .value_kind:     global_buffer
    .group_segment_fixed_size: 0
    .kernarg_segment_align: 8
    .kernarg_segment_size: 16
    .language:       OpenCL C
    .language_version:
      - 2
      - 0
    .max_flat_workgroup_size: 256
    .name:           _Z13reduce_kernelPKDF16_Pf
    .private_segment_fixed_size: 0
    .sgpr_count:     25
    .sgpr_spill_count: 0
    .symbol:         _Z13reduce_kernelPKDF16_Pf.kd
    .uniform_work_group_size: 1
    .uses_dynamic_stack: false
    .vgpr_count:     78
    .vgpr_spill_count: 0
    .wavefront_size: 64
